# remaining narrow flat stores (dword/dwordx2) also replaced by global stores
# baseline (speedup 1.0000x reference)
.LBB0_228:
	s_add_i32 s7, s97, s6
	s_cmpk_lt_i32 s7, 0x4000
	s_cselect_b32 s8, s7, s6
	s_ashr_i32 s9, s8, 31
	v_mad_i64_i32 v[44:45], s[10:11], s8, v194, v[18:19]
	s_lshl_b64 s[8:9], s[8:9], 2
	s_add_u32 s8, s23, s8
	s_addc_u32 s9, s22, s9
	flat_load_dword v96, v[44:45]
	flat_load_dword v95, v[44:45] offset:256
	flat_load_dword v94, v[44:45] offset:512
	flat_load_dword v93, v[44:45] offset:768
	s_waitcnt lgkmcnt(0)
	flat_load_dword v92, v[44:45] offset:1024
	flat_load_dword v90, v[44:45] offset:1280
	v_mov_b64_e32 v[44:45], s[8:9]
	v_readlane_b32 s8, v239, 54
	s_add_i32 s18, s8, s6
	s_cmpk_lt_i32 s18, 0x4000
	s_cselect_b32 s8, s18, s6
	s_ashr_i32 s9, s8, 31
	flat_load_dword v91, v[44:45]
	v_mad_i64_i32 v[44:45], s[10:11], s8, v194, v[18:19]
	s_lshl_b64 s[8:9], s[8:9], 2
	s_add_u32 s8, s23, s8
	s_addc_u32 s9, s22, s9
	flat_load_dword v89, v[44:45]
	flat_load_dword v88, v[44:45] offset:256
	flat_load_dword v87, v[44:45] offset:512
	flat_load_dword v86, v[44:45] offset:768
	flat_load_dword v85, v[44:45] offset:1024
	flat_load_dword v78, v[44:45] offset:1280
	v_mov_b64_e32 v[44:45], s[8:9]
	s_mul_i32 s8, s87, 24
	s_add_i32 s16, s8, s6
	s_cmpk_lt_i32 s16, 0x4000
	s_cselect_b32 s8, s16, s6
	flat_load_dword v79, v[44:45]
	v_mad_i64_i32 v[44:45], s[10:11], s8, v194, v[18:19]
	v_lshl_add_u64 v[46:47], s[78:79], 0, v[34:35]
	s_mov_b32 s10, 0x8200000
	v_add_co_u32_e32 v46, vcc, s10, v46
	s_ashr_i32 s9, s8, 31
	s_nop 0
	v_addc_co_u32_e32 v47, vcc, 0, v47, vcc
	flat_load_dword v97, v[46:47] offset:1280
	flat_load_dword v110, v[46:47] offset:1024
	flat_load_dword v105, v[46:47] offset:768
	flat_load_dword v103, v[46:47] offset:512
	flat_load_dword v99, v[46:47] offset:256
	s_nop 0
	flat_load_dword v47, v[46:47]
	s_nop 0
	flat_load_dword v84, v[44:45]
	flat_load_dword v83, v[44:45] offset:256
	flat_load_dword v82, v[44:45] offset:512
	flat_load_dword v81, v[44:45] offset:768
	flat_load_dword v80, v[44:45] offset:1024
	flat_load_dword v76, v[44:45] offset:1280
	s_lshl_b64 s[8:9], s[8:9], 2
	s_add_u32 s8, s23, s8
	s_addc_u32 s9, s22, s9
	s_add_i32 s14, s70, s6
	s_cmpk_lt_i32 s14, 0x4000
	v_mov_b64_e32 v[44:45], s[8:9]
	s_cselect_b32 s8, s14, s6
	s_ashr_i32 s9, s8, 31
	flat_load_dword v77, v[44:45]
	v_mad_i64_i32 v[44:45], s[10:11], s8, v194, v[18:19]
	s_lshl_b64 s[8:9], s[8:9], 2
	s_add_u32 s8, s23, s8
	s_addc_u32 s9, s22, s9
	flat_load_dword v75, v[44:45]
	flat_load_dword v74, v[44:45] offset:256
	flat_load_dword v73, v[44:45] offset:512
	flat_load_dword v72, v[44:45] offset:768
	flat_load_dword v71, v[44:45] offset:1024
	flat_load_dword v69, v[44:45] offset:1280
	v_mov_b64_e32 v[44:45], s[8:9]
	s_mul_i32 s8, s87, 40
	s_add_i32 s12, s8, s6
	s_cmpk_lt_i32 s12, 0x4000
	s_cselect_b32 s8, s12, s6
	s_ashr_i32 s9, s8, 31
	flat_load_dword v70, v[44:45]
	v_mad_i64_i32 v[44:45], s[10:11], s8, v194, v[18:19]
	s_lshl_b64 s[8:9], s[8:9], 2
	s_add_u32 s8, s23, s8
	s_addc_u32 s9, s22, s9
	flat_load_dword v68, v[44:45]
	flat_load_dword v67, v[44:45] offset:256
	flat_load_dword v66, v[44:45] offset:512
	flat_load_dword v65, v[44:45] offset:768
	flat_load_dword v64, v[44:45] offset:1024
	flat_load_dword v62, v[44:45] offset:1280
	v_mov_b64_e32 v[44:45], s[8:9]
	s_mul_i32 s8, s87, 48
	s_add_i32 s10, s8, s6
	s_cmpk_lt_i32 s10, 0x4000
	s_cselect_b32 s8, s10, s6
	s_ashr_i32 s9, s8, 31
	flat_load_dword v63, v[44:45]
	v_mad_i64_i32 v[44:45], s[20:21], s8, v194, v[18:19]
	s_lshl_b64 s[8:9], s[8:9], 2
	s_add_u32 s8, s23, s8
	s_addc_u32 s9, s22, s9
	flat_load_dword v61, v[44:45]
	flat_load_dword v60, v[44:45] offset:256
	flat_load_dword v59, v[44:45] offset:512
	flat_load_dword v58, v[44:45] offset:768
	flat_load_dword v57, v[44:45] offset:1024
	flat_load_dword v55, v[44:45] offset:1280
	v_mov_b64_e32 v[44:45], s[8:9]
	s_mul_i32 s8, s87, 56
	s_add_i32 s8, s8, s6
	s_cmpk_lt_i32 s8, 0x4000
	s_cselect_b32 s20, s8, s6
	s_ashr_i32 s21, s20, 31
	flat_load_dword v56, v[44:45]
	v_mad_i64_i32 v[44:45], s[24:25], s20, v194, v[18:19]
	s_lshl_b64 s[20:21], s[20:21], 2
	flat_load_dword v54, v[44:45]
	flat_load_dword v53, v[44:45] offset:256
	flat_load_dword v52, v[44:45] offset:512
	flat_load_dword v51, v[44:45] offset:768
	flat_load_dword v50, v[44:45] offset:1024
	flat_load_dword v48, v[44:45] offset:1280
	s_add_u32 s20, s23, s20
	s_addc_u32 s21, s22, s21
	v_mov_b64_e32 v[44:45], s[20:21]
	flat_load_dword v49, v[44:45]
	v_mov_b64_e32 v[44:45], s[0:1]
	flat_load_dword v44, v[44:45]
	s_waitcnt vmcnt(0) lgkmcnt(0)
	v_lshlrev_b32_e32 v104, 16, v105
	v_lshlrev_b32_e32 v102, 16, v103
	v_and_b32_e32 v103, 0xffff0000, v103
	v_lshlrev_b32_e32 v46, 16, v47
	v_and_b32_e32 v47, 0xffff0000, v47
	v_lshlrev_b32_e32 v98, 16, v99
	v_and_b32_e32 v99, 0xffff0000, v99
	v_mov_b32_e32 v106, v47
	v_mov_b32_e32 v107, v103
	v_pk_mul_f32 v[100:101], v[98:99], v[98:99]
	v_pk_mul_f32 v[106:107], v[106:107], v[106:107]
	v_mov_b32_e32 v108, v46
	v_mov_b32_e32 v109, v102
	v_pk_fma_f32 v[106:107], v[108:109], v[108:109], v[106:107]
	v_add_f32_e32 v45, v100, v101
	v_add_f32_e32 v45, v106, v45
	v_add_f32_e32 v45, v45, v107
	v_lshl_add_u64 v[108:109], s[78:79], 0, v[32:33]
	v_and_b32_e32 v105, 0xffff0000, v105
	v_add_f32_dpp v45, v45, v45 quad_perm:[1,0,3,2] row_mask:0xf bank_mask:0xf bound_ctrl:1
	v_and_b32_e32 v107, 0xffff0000, v110
	v_lshlrev_b32_e32 v106, 16, v110
	v_add_f32_dpp v45, v45, v45 quad_perm:[2,3,0,1] row_mask:0xf bank_mask:0xf bound_ctrl:1
	s_nop 1
	v_add_f32_dpp v45, v45, v45 row_half_mirror row_mask:0xf bank_mask:0xf bound_ctrl:1
	s_nop 1
	v_add_f32_dpp v45, v45, v45 row_mirror row_mask:0xf bank_mask:0xf bound_ctrl:1
	s_nop 0
	v_readlane_b32 s9, v45, 16
	v_readlane_b32 s11, v45, 48
	v_readlane_b32 s20, v45, 0
	v_readlane_b32 s21, v45, 32
	v_mov_b32_e32 v100, s9
	v_mov_b32_e32 v101, s11
	v_pk_add_f32 v[100:101], s[20:21], v[100:101]
	s_mov_b32 s9, 0x9a00000
	v_add_f32_e32 v45, v100, v101
	v_fmamk_f32 v45, v45, 0x3b2aaaab, v189
	v_rsq_f32_e32 v100, v45
	s_nop 0
	v_pk_mul_f32 v[46:47], v[100:101], v[46:47] op_sel_hi:[0,1]
	v_pk_mul_f32 v[46:47], v[2:3], v[46:47]
	v_pk_mul_f32 v[98:99], v[100:101], v[98:99] op_sel_hi:[0,1]
	v_cvt_pk_bf16_f32 v45, v46, v47
	v_add_co_u32_e32 v46, vcc, s9, v108
	v_pk_mul_f32 v[98:99], v[4:5], v[98:99]
	s_nop 0
	v_addc_co_u32_e32 v47, vcc, 0, v109, vcc
	global_store_dword v[46:47], v45, off
	v_cvt_pk_bf16_f32 v45, v98, v99
	v_pk_mul_f32 v[98:99], v[100:101], v[102:103] op_sel_hi:[0,1]
	v_mov_b32_e32 v102, v105
	v_mov_b32_e32 v103, v107
	v_mov_b32_e32 v100, v104
	v_mov_b32_e32 v101, v106
	v_pk_mul_f32 v[102:103], v[102:103], v[102:103]
	global_store_dword v[46:47], v45, off offset:256
	v_pk_fma_f32 v[100:101], v[100:101], v[100:101], v[102:103]
	v_pk_mul_f32 v[98:99], v[6:7], v[98:99]
	v_add_f32_e32 v45, v100, v101
	s_nop 1
	v_add_f32_dpp v45, v45, v45 quad_perm:[1,0,3,2] row_mask:0xf bank_mask:0xf bound_ctrl:1
	s_nop 1
	v_add_f32_dpp v45, v45, v45 quad_perm:[2,3,0,1] row_mask:0xf bank_mask:0xf bound_ctrl:1
	s_nop 1
	v_add_f32_dpp v45, v45, v45 row_half_mirror row_mask:0xf bank_mask:0xf bound_ctrl:1
	s_nop 1
	v_add_f32_dpp v45, v45, v45 row_mirror row_mask:0xf bank_mask:0xf bound_ctrl:1
	s_nop 0
	v_readlane_b32 s9, v45, 16
	v_readlane_b32 s11, v45, 48
	v_readlane_b32 s20, v45, 0
	v_readlane_b32 s21, v45, 32
	v_mov_b32_e32 v100, s9
	v_mov_b32_e32 v101, s11
	v_pk_add_f32 v[100:101], s[20:21], v[100:101]
	s_nop 0
	v_add_f32_e32 v45, v100, v101
	v_fmamk_f32 v45, v45, 0x3b800000, v189
	v_rsq_f32_e32 v100, v45
	v_cvt_pk_bf16_f32 v45, v98, v99
	global_store_dword v[46:47], v45, off offset:512
	v_lshl_add_u64 v[46:47], s[78:79], 0, v[30:31]
	v_pk_mul_f32 v[98:99], v[100:101], v[104:105] op_sel_hi:[0,1]
	v_pk_mul_f32 v[98:99], v[8:9], v[98:99]
	v_add_co_u32_e32 v46, vcc, 0xa600000, v46
	v_cvt_pk_bf16_f32 v45, v98, v99
	ds_bpermute_b32 v98, v1, v97
	v_pk_mul_f32 v[100:101], v[100:101], v[106:107] op_sel_hi:[0,1]
	v_addc_co_u32_e32 v47, vcc, 0, v47, vcc
	v_pk_mul_f32 v[100:101], v[10:11], v[100:101]
	global_store_dword v[46:47], v45, off
	v_cvt_pk_bf16_f32 v45, v100, v101
	global_store_dword v[46:47], v45, off offset:256
	s_and_saveexec_b64 s[20:21], s[2:3]
	s_cbranch_execz .LBB0_231
	v_cvt_f32_i32_e32 v44, v44
	s_mov_b32 s24, 0x6dc9c883
	s_mov_b32 s25, 0x3fc45f30
	s_waitcnt lgkmcnt(0)
	v_and_b32_e32 v99, 0xffff0000, v98
	v_cvt_f64_f32_e32 v[44:45], v44
	v_mul_f64 v[46:47], v[12:13], v[44:45]
	v_mul_f64 v[44:45], v[14:15], v[44:45]
	v_mul_f64 v[100:101], v[46:47], s[24:25]
	v_mul_f64 v[102:103], v[44:45], s[24:25]
	v_rndne_f64_e32 v[100:101], v[100:101]
	v_rndne_f64_e32 v[102:103], v[102:103]
	v_fma_f64 v[46:47], v[46:47], s[24:25], -v[100:101]
	v_fma_f64 v[44:45], v[44:45], s[24:25], -v[102:103]
	v_cvt_f32_f64_e32 v47, v[46:47]
	v_cvt_f32_f64_e32 v45, v[44:45]
	v_cos_f32_e32 v46, v47
	v_sin_f32_e32 v44, v47
	v_cos_f32_e32 v47, v45
	v_sin_f32_e32 v45, v45
	v_lshlrev_b32_e32 v98, 16, v98
	v_lshlrev_b32_e32 v100, 16, v97
	v_and_b32_e32 v101, 0xffff0000, v97
	v_pk_mul_f32 v[98:99], v[44:45], v[98:99]
	s_nop 0
	v_cndmask_b32_e64 v99, v99, -v99, s[4:5]
	v_cndmask_b32_e64 v98, v98, -v98, s[4:5]
	v_pk_fma_f32 v[98:99], v[46:47], v[100:101], v[98:99]
	s_nop 0
	v_cvt_pk_bf16_f32 v97, v98, v99
	v_lshl_add_u64 v[98:99], s[78:79], 0, v[28:29]
	global_store_dword v[98:99], v97, off
	s_and_b64 exec, exec, s[4:5]
	s_cbranch_execz .LBB0_231
	v_lshl_add_u64 v[98:99], s[78:79], 0, v[26:27]
	v_add_co_u32_e32 v98, vcc, 0xb000000, v98
	s_nop 1
	v_addc_co_u32_e32 v99, vcc, 0, v99, vcc
	global_store_dwordx2 v[98:99], v[46:47], off
	global_store_dwordx2 v[98:99], v[44:45], off offset:128
.LBB0_231:
	s_or_b64 exec, exec, s[20:21]
	s_cmpk_gt_i32 s7, 0x3fff
	s_cbranch_scc1 .LBB0_247
	v_and_b32_e32 v45, 0xffff0000, v96
	v_and_b32_e32 v99, 0xffff0000, v94
	v_lshlrev_b32_e32 v44, 16, v96
	v_lshlrev_b32_e32 v46, 16, v95
	v_and_b32_e32 v47, 0xffff0000, v95
	s_waitcnt lgkmcnt(0)
	v_lshlrev_b32_e32 v98, 16, v94
	v_mov_b32_e32 v100, v45
	v_mov_b32_e32 v101, v99
	v_pk_mul_f32 v[96:97], v[46:47], v[46:47]
	v_pk_mul_f32 v[100:101], v[100:101], v[100:101]
	v_mov_b32_e32 v102, v44
	v_mov_b32_e32 v103, v98
	v_lshlrev_b32_e32 v94, 16, v93
	v_and_b32_e32 v95, 0xffff0000, v93
	v_pk_fma_f32 v[100:101], v[102:103], v[102:103], v[100:101]
	v_add_f32_e32 v93, v96, v97
	v_add_f32_e32 v93, v100, v93
	v_add_f32_e32 v93, v93, v101
	v_lshlrev_b32_e32 v100, 16, v92
	v_and_b32_e32 v101, 0xffff0000, v92
	v_add_f32_dpp v93, v93, v93 quad_perm:[1,0,3,2] row_mask:0xf bank_mask:0xf bound_ctrl:1
	s_nop 1
	v_add_f32_dpp v93, v93, v93 quad_perm:[2,3,0,1] row_mask:0xf bank_mask:0xf bound_ctrl:1
	s_nop 1
	v_add_f32_dpp v93, v93, v93 row_half_mirror row_mask:0xf bank_mask:0xf bound_ctrl:1
	s_nop 1
	v_add_f32_dpp v93, v93, v93 row_mirror row_mask:0xf bank_mask:0xf bound_ctrl:1
	s_nop 0
	v_readlane_b32 s7, v93, 16
	v_readlane_b32 s9, v93, 48
	v_readlane_b32 s20, v93, 0
	v_readlane_b32 s21, v93, 32
	v_mov_b32_e32 v96, s7
	v_mov_b32_e32 v97, s9
	v_pk_add_f32 v[96:97], s[20:21], v[96:97]
	s_mov_b32 s7, 0x9a00000
	v_add_f32_e32 v93, v96, v97
	v_fmamk_f32 v93, v93, 0x3b2aaaab, v189
	v_rsq_f32_e32 v96, v93
	v_lshl_add_u64 v[92:93], s[78:79], 0, v[42:43]
	v_pk_mul_f32 v[44:45], v[96:97], v[44:45] op_sel_hi:[0,1]
	v_pk_mul_f32 v[44:45], v[2:3], v[44:45]
	s_nop 0
	v_cvt_pk_bf16_f32 v97, v44, v45
	v_pk_mul_f32 v[46:47], v[96:97], v[46:47] op_sel_hi:[0,1]
	v_add_co_u32_e32 v44, vcc, s7, v92
	v_pk_mul_f32 v[46:47], v[4:5], v[46:47]
	s_nop 0
	v_addc_co_u32_e32 v45, vcc, 0, v93, vcc
	v_cvt_pk_bf16_f32 v46, v46, v47
	global_store_dword v[44:45], v97, off
	global_store_dword v[44:45], v46, off offset:256
	v_pk_mul_f32 v[46:47], v[96:97], v[98:99] op_sel_hi:[0,1]
	v_mov_b32_e32 v96, v95
	v_mov_b32_e32 v97, v101
	v_mov_b32_e32 v92, v94
	v_mov_b32_e32 v93, v100
	v_pk_mul_f32 v[96:97], v[96:97], v[96:97]
	v_pk_mul_f32 v[46:47], v[6:7], v[46:47]
	v_pk_fma_f32 v[92:93], v[92:93], v[92:93], v[96:97]
	v_cvt_pk_bf16_f32 v46, v46, v47
	v_add_f32_e32 v92, v92, v93
	global_store_dword v[44:45], v46, off offset:512
	v_lshl_add_u64 v[44:45], s[78:79], 0, v[40:41]
	v_add_f32_dpp v92, v92, v92 quad_perm:[1,0,3,2] row_mask:0xf bank_mask:0xf bound_ctrl:1
	v_add_co_u32_e32 v44, vcc, 0xa600000, v44
	s_nop 0
	v_add_f32_dpp v92, v92, v92 quad_perm:[2,3,0,1] row_mask:0xf bank_mask:0xf bound_ctrl:1
	v_addc_co_u32_e32 v45, vcc, 0, v45, vcc
	s_nop 0
	v_add_f32_dpp v92, v92, v92 row_half_mirror row_mask:0xf bank_mask:0xf bound_ctrl:1
	s_nop 1
	v_add_f32_dpp v92, v92, v92 row_mirror row_mask:0xf bank_mask:0xf bound_ctrl:1
	s_nop 0
	v_readlane_b32 s7, v92, 16
	v_readlane_b32 s9, v92, 48
	v_readlane_b32 s20, v92, 0
	v_readlane_b32 s21, v92, 32
	v_mov_b32_e32 v92, s7
	v_mov_b32_e32 v93, s9
	v_pk_add_f32 v[92:93], s[20:21], v[92:93]
	s_nop 0
	v_add_f32_e32 v92, v92, v93
	v_fmamk_f32 v92, v92, 0x3b800000, v189
	v_rsq_f32_e32 v96, v92
	ds_bpermute_b32 v92, v1, v90
	v_pk_mul_f32 v[46:47], v[96:97], v[94:95] op_sel_hi:[0,1]
	v_pk_mul_f32 v[46:47], v[8:9], v[46:47]
	s_nop 0
	v_cvt_pk_bf16_f32 v46, v46, v47
	global_store_dword v[44:45], v46, off
	v_pk_mul_f32 v[46:47], v[96:97], v[100:101] op_sel_hi:[0,1]
	v_pk_mul_f32 v[46:47], v[10:11], v[46:47]
	s_nop 0
	v_cvt_pk_bf16_f32 v46, v46, v47
	global_store_dword v[44:45], v46, off offset:256
	s_and_saveexec_b64 s[20:21], s[2:3]
	s_cbranch_execz .LBB0_235
	v_cvt_f32_i32_e32 v44, v91
	s_mov_b32 s24, 0x6dc9c883
	s_mov_b32 s25, 0x3fc45f30
	s_waitcnt lgkmcnt(0)
	v_and_b32_e32 v93, 0xffff0000, v92
	v_cvt_f64_f32_e32 v[44:45], v44
	v_mul_f64 v[46:47], v[12:13], v[44:45]
	v_mul_f64 v[44:45], v[14:15], v[44:45]
	v_mul_f64 v[94:95], v[46:47], s[24:25]
	v_mul_f64 v[96:97], v[44:45], s[24:25]
	v_rndne_f64_e32 v[94:95], v[94:95]
	v_rndne_f64_e32 v[96:97], v[96:97]
	v_fma_f64 v[46:47], v[46:47], s[24:25], -v[94:95]
	v_fma_f64 v[44:45], v[44:45], s[24:25], -v[96:97]
	v_cvt_f32_f64_e32 v47, v[46:47]
	v_cvt_f32_f64_e32 v45, v[44:45]
	v_cos_f32_e32 v46, v47
	v_sin_f32_e32 v44, v47
	v_cos_f32_e32 v47, v45
	v_sin_f32_e32 v45, v45
	v_lshlrev_b32_e32 v92, 16, v92
	v_lshlrev_b32_e32 v94, 16, v90
	v_and_b32_e32 v95, 0xffff0000, v90
	v_pk_mul_f32 v[90:91], v[44:45], v[92:93]
	s_nop 0
	v_cndmask_b32_e64 v91, v91, -v91, s[4:5]
	v_cndmask_b32_e64 v90, v90, -v90, s[4:5]
	v_pk_fma_f32 v[90:91], v[46:47], v[94:95], v[90:91]
	s_nop 0
	v_cvt_pk_bf16_f32 v92, v90, v91
	v_lshl_add_u64 v[90:91], s[78:79], 0, v[38:39]
	global_store_dword v[90:91], v92, off
	s_and_b64 exec, exec, s[4:5]
	s_cbranch_execz .LBB0_235
	v_lshl_add_u64 v[90:91], s[78:79], 0, v[36:37]
	v_add_co_u32_e32 v90, vcc, 0xb000000, v90
	s_nop 1
	v_addc_co_u32_e32 v91, vcc, 0, v91, vcc
	global_store_dwordx2 v[90:91], v[46:47], off
	global_store_dwordx2 v[90:91], v[44:45], off offset:128

.LBB0_237:
	v_and_b32_e32 v45, 0xffff0000, v84
	s_waitcnt lgkmcnt(0)
	v_and_b32_e32 v85, 0xffff0000, v82
	v_lshlrev_b32_e32 v44, 16, v84
	v_lshlrev_b32_e32 v46, 16, v83
	v_and_b32_e32 v47, 0xffff0000, v83
	v_lshlrev_b32_e32 v84, 16, v82
	v_lshlrev_b32_e32 v82, 16, v81
	v_and_b32_e32 v83, 0xffff0000, v81
	v_lshlrev_b32_e32 v86, 16, v80
	v_and_b32_e32 v87, 0xffff0000, v80
	v_mov_b32_e32 v80, v45
	v_mov_b32_e32 v81, v85
	v_pk_mul_f32 v[78:79], v[46:47], v[46:47]
	v_pk_mul_f32 v[80:81], v[80:81], v[80:81]
	v_mov_b32_e32 v88, v44
	v_mov_b32_e32 v89, v84
	v_pk_fma_f32 v[80:81], v[88:89], v[88:89], v[80:81]
	v_add_f32_e32 v78, v78, v79
	v_add_f32_e32 v78, v80, v78
	v_add_f32_e32 v78, v78, v81
	s_ashr_i32 s17, s16, 31
	s_nop 0
	v_add_f32_dpp v78, v78, v78 quad_perm:[1,0,3,2] row_mask:0xf bank_mask:0xf bound_ctrl:1
	s_nop 1
	v_add_f32_dpp v78, v78, v78 quad_perm:[2,3,0,1] row_mask:0xf bank_mask:0xf bound_ctrl:1
	s_nop 1
	v_add_f32_dpp v78, v78, v78 row_half_mirror row_mask:0xf bank_mask:0xf bound_ctrl:1
	s_nop 1
	v_add_f32_dpp v78, v78, v78 row_mirror row_mask:0xf bank_mask:0xf bound_ctrl:1
	s_nop 0
	v_readlane_b32 s7, v78, 16
	v_readlane_b32 s9, v78, 48
	v_readlane_b32 s18, v78, 0
	v_readlane_b32 s19, v78, 32
	v_mov_b32_e32 v78, s7
	v_mov_b32_e32 v79, s9
	v_pk_add_f32 v[78:79], s[18:19], v[78:79]
	v_mad_i64_i32 v[80:81], s[18:19], s16, v193, v[20:21]
	v_add_f32_e32 v78, v78, v79
	v_fmamk_f32 v78, v78, 0x3b2aaaab, v189
	v_rsq_f32_e32 v78, v78
	s_nop 0
	v_pk_mul_f32 v[44:45], v[78:79], v[44:45] op_sel_hi:[0,1]
	v_pk_mul_f32 v[44:45], v[2:3], v[44:45]
	s_nop 0
	v_cvt_pk_bf16_f32 v44, v44, v45
	global_store_dword v[80:81], v44, off
	v_pk_mul_f32 v[44:45], v[78:79], v[46:47] op_sel_hi:[0,1]
	v_pk_mul_f32 v[44:45], v[4:5], v[44:45]
	v_mov_b32_e32 v46, v83
	v_cvt_pk_bf16_f32 v44, v44, v45
	global_store_dword v[80:81], v44, off offset:256
	v_pk_mul_f32 v[44:45], v[78:79], v[84:85] op_sel_hi:[0,1]
	v_pk_mul_f32 v[44:45], v[6:7], v[44:45]
	v_mov_b32_e32 v47, v87
	v_cvt_pk_bf16_f32 v78, v44, v45
	v_mov_b32_e32 v44, v82
	v_mov_b32_e32 v45, v86
	v_pk_mul_f32 v[46:47], v[46:47], v[46:47]
	global_store_dword v[80:81], v78, off offset:512
	v_pk_fma_f32 v[44:45], v[44:45], v[44:45], v[46:47]
	s_nop 0
	v_add_f32_e32 v44, v44, v45
	s_nop 1
	v_add_f32_dpp v44, v44, v44 quad_perm:[1,0,3,2] row_mask:0xf bank_mask:0xf bound_ctrl:1
	s_nop 1
	v_add_f32_dpp v44, v44, v44 quad_perm:[2,3,0,1] row_mask:0xf bank_mask:0xf bound_ctrl:1
	s_nop 1
	v_add_f32_dpp v44, v44, v44 row_half_mirror row_mask:0xf bank_mask:0xf bound_ctrl:1
	s_nop 1
	v_add_f32_dpp v44, v44, v44 row_mirror row_mask:0xf bank_mask:0xf bound_ctrl:1
	s_nop 0
	v_readlane_b32 s7, v44, 16
	v_readlane_b32 s9, v44, 48
	v_readlane_b32 s18, v44, 0
	v_readlane_b32 s19, v44, 32
	v_mov_b32_e32 v44, s7
	v_mov_b32_e32 v45, s9
	v_pk_add_f32 v[44:45], s[18:19], v[44:45]
	s_lshl_b64 s[18:19], s[16:17], 9
	v_add_f32_e32 v44, v44, v45
	v_fmamk_f32 v44, v44, 0x3b800000, v189
	v_rsq_f32_e32 v44, v44
	v_lshl_add_u64 v[46:47], v[22:23], 0, s[18:19]
	v_pk_mul_f32 v[78:79], v[44:45], v[82:83] op_sel_hi:[0,1]
	v_pk_mul_f32 v[78:79], v[8:9], v[78:79]
	s_nop 0
	v_cvt_pk_bf16_f32 v45, v78, v79
	ds_bpermute_b32 v78, v1, v76
	global_store_dword v[46:47], v45, off
	v_pk_mul_f32 v[44:45], v[44:45], v[86:87] op_sel_hi:[0,1]
	v_pk_mul_f32 v[44:45], v[10:11], v[44:45]
	s_nop 0
	v_cvt_pk_bf16_f32 v44, v44, v45
	global_store_dword v[46:47], v44, off offset:256
	s_and_saveexec_b64 s[18:19], s[2:3]
	s_cbranch_execz .LBB0_240
	v_cvt_f32_i32_e32 v44, v77
	s_mov_b32 s20, 0x6dc9c883
	s_mov_b32 s21, 0x3fc45f30
	s_waitcnt lgkmcnt(0)
	v_and_b32_e32 v79, 0xffff0000, v78
	v_cvt_f64_f32_e32 v[44:45], v44
	v_mul_f64 v[46:47], v[12:13], v[44:45]
	v_mul_f64 v[44:45], v[14:15], v[44:45]
	v_mul_f64 v[80:81], v[46:47], s[20:21]
	v_mul_f64 v[82:83], v[44:45], s[20:21]
	v_rndne_f64_e32 v[80:81], v[80:81]
	v_rndne_f64_e32 v[82:83], v[82:83]
	v_fma_f64 v[46:47], v[46:47], s[20:21], -v[80:81]
	v_fma_f64 v[44:45], v[44:45], s[20:21], -v[82:83]
	v_cvt_f32_f64_e32 v47, v[46:47]
	v_cvt_f32_f64_e32 v45, v[44:45]
	v_cos_f32_e32 v46, v47
	v_sin_f32_e32 v44, v47
	v_cos_f32_e32 v47, v45
	v_sin_f32_e32 v45, v45
	v_lshlrev_b32_e32 v78, 16, v78
	v_lshlrev_b32_e32 v80, 16, v76
	v_and_b32_e32 v81, 0xffff0000, v76
	v_pk_mul_f32 v[76:77], v[44:45], v[78:79]
	s_lshl_b64 s[20:21], s[16:17], 7
	v_cndmask_b32_e64 v77, v77, -v77, s[4:5]
	v_cndmask_b32_e64 v76, v76, -v76, s[4:5]
	v_pk_fma_f32 v[76:77], v[46:47], v[80:81], v[76:77]
	s_nop 0
	v_cvt_pk_bf16_f32 v78, v76, v77
	v_lshl_add_u64 v[76:77], v[16:17], 0, s[20:21]
	global_store_dword v[76:77], v78, off
	s_and_b64 exec, exec, s[4:5]
	s_cbranch_execz .LBB0_240
	s_lshl_b64 s[16:17], s[16:17], 6
	v_lshl_add_u64 v[76:77], s[16:17], 2, v[24:25]
	global_store_dwordx2 v[76:77], v[46:47], off
	global_store_dwordx2 v[76:77], v[44:45], off offset:128

.LBB0_242:
	v_and_b32_e32 v45, 0xffff0000, v68
	s_waitcnt lgkmcnt(0)
	v_and_b32_e32 v71, 0xffff0000, v66
	v_lshlrev_b32_e32 v44, 16, v68
	v_lshlrev_b32_e32 v46, 16, v67
	v_and_b32_e32 v47, 0xffff0000, v67
	v_lshlrev_b32_e32 v70, 16, v66
	v_lshlrev_b32_e32 v66, 16, v65
	v_and_b32_e32 v67, 0xffff0000, v65
	v_lshlrev_b32_e32 v72, 16, v64
	v_and_b32_e32 v73, 0xffff0000, v64
	v_mov_b32_e32 v64, v45
	v_mov_b32_e32 v65, v71
	v_pk_mul_f32 v[68:69], v[46:47], v[46:47]
	v_pk_mul_f32 v[64:65], v[64:65], v[64:65]
	v_mov_b32_e32 v74, v44
	v_mov_b32_e32 v75, v70
	v_pk_fma_f32 v[64:65], v[74:75], v[74:75], v[64:65]
	v_add_f32_e32 v68, v68, v69
	v_add_f32_e32 v64, v64, v68
	v_add_f32_e32 v64, v64, v65
	s_ashr_i32 s13, s12, 31
	s_nop 0
	v_add_f32_dpp v64, v64, v64 quad_perm:[1,0,3,2] row_mask:0xf bank_mask:0xf bound_ctrl:1
	s_nop 1
	v_add_f32_dpp v64, v64, v64 quad_perm:[2,3,0,1] row_mask:0xf bank_mask:0xf bound_ctrl:1
	s_nop 1
	v_add_f32_dpp v64, v64, v64 row_half_mirror row_mask:0xf bank_mask:0xf bound_ctrl:1
	s_nop 1
	v_add_f32_dpp v64, v64, v64 row_mirror row_mask:0xf bank_mask:0xf bound_ctrl:1
	s_nop 0
	v_readlane_b32 s7, v64, 16
	v_readlane_b32 s9, v64, 48
	v_readlane_b32 s14, v64, 0
	v_readlane_b32 s15, v64, 32
	v_mov_b32_e32 v64, s7
	v_mov_b32_e32 v65, s9
	v_pk_add_f32 v[64:65], s[14:15], v[64:65]
	v_mad_i64_i32 v[68:69], s[14:15], s12, v193, v[20:21]
	v_add_f32_e32 v64, v64, v65
	v_fmamk_f32 v64, v64, 0x3b2aaaab, v189
	v_rsq_f32_e32 v64, v64
	s_nop 0
	v_pk_mul_f32 v[44:45], v[64:65], v[44:45] op_sel_hi:[0,1]
	v_pk_mul_f32 v[44:45], v[2:3], v[44:45]
	s_nop 0
	v_cvt_pk_bf16_f32 v44, v44, v45
	global_store_dword v[68:69], v44, off
	v_pk_mul_f32 v[44:45], v[64:65], v[46:47] op_sel_hi:[0,1]
	v_pk_mul_f32 v[44:45], v[4:5], v[44:45]
	v_mov_b32_e32 v46, v67
	v_cvt_pk_bf16_f32 v44, v44, v45
	global_store_dword v[68:69], v44, off offset:256
	v_pk_mul_f32 v[44:45], v[64:65], v[70:71] op_sel_hi:[0,1]
	v_pk_mul_f32 v[44:45], v[6:7], v[44:45]
	v_mov_b32_e32 v47, v73
	v_cvt_pk_bf16_f32 v64, v44, v45
	v_mov_b32_e32 v44, v66
	v_mov_b32_e32 v45, v72
	v_pk_mul_f32 v[46:47], v[46:47], v[46:47]
	global_store_dword v[68:69], v64, off offset:512
	v_pk_fma_f32 v[44:45], v[44:45], v[44:45], v[46:47]
	s_nop 0
	v_add_f32_e32 v44, v44, v45
	s_nop 1
	v_add_f32_dpp v44, v44, v44 quad_perm:[1,0,3,2] row_mask:0xf bank_mask:0xf bound_ctrl:1
	s_nop 1
	v_add_f32_dpp v44, v44, v44 quad_perm:[2,3,0,1] row_mask:0xf bank_mask:0xf bound_ctrl:1
	s_nop 1
	v_add_f32_dpp v44, v44, v44 row_half_mirror row_mask:0xf bank_mask:0xf bound_ctrl:1
	s_nop 1
	v_add_f32_dpp v44, v44, v44 row_mirror row_mask:0xf bank_mask:0xf bound_ctrl:1
	s_nop 0
	v_readlane_b32 s7, v44, 16
	v_readlane_b32 s9, v44, 48
	v_readlane_b32 s14, v44, 0
	v_readlane_b32 s15, v44, 32
	v_mov_b32_e32 v44, s7
	v_mov_b32_e32 v45, s9
	v_pk_add_f32 v[44:45], s[14:15], v[44:45]
	s_lshl_b64 s[14:15], s[12:13], 9
	v_add_f32_e32 v44, v44, v45
	v_fmamk_f32 v44, v44, 0x3b800000, v189
	v_rsq_f32_e32 v44, v44
	v_lshl_add_u64 v[46:47], v[22:23], 0, s[14:15]
	v_pk_mul_f32 v[64:65], v[44:45], v[66:67] op_sel_hi:[0,1]
	v_pk_mul_f32 v[64:65], v[8:9], v[64:65]
	s_nop 0
	v_cvt_pk_bf16_f32 v45, v64, v65
	ds_bpermute_b32 v64, v1, v62
	global_store_dword v[46:47], v45, off
	v_pk_mul_f32 v[44:45], v[44:45], v[72:73] op_sel_hi:[0,1]
	v_pk_mul_f32 v[44:45], v[10:11], v[44:45]
	s_nop 0
	v_cvt_pk_bf16_f32 v44, v44, v45
	global_store_dword v[46:47], v44, off offset:256
	s_and_saveexec_b64 s[14:15], s[2:3]
	s_cbranch_execz .LBB0_245
	v_cvt_f32_i32_e32 v44, v63
	s_mov_b32 s16, 0x6dc9c883
	s_mov_b32 s17, 0x3fc45f30
	s_waitcnt lgkmcnt(0)
	v_and_b32_e32 v65, 0xffff0000, v64
	v_cvt_f64_f32_e32 v[44:45], v44
	v_mul_f64 v[46:47], v[12:13], v[44:45]
	v_mul_f64 v[44:45], v[14:15], v[44:45]
	v_mul_f64 v[66:67], v[46:47], s[16:17]
	v_mul_f64 v[68:69], v[44:45], s[16:17]
	v_rndne_f64_e32 v[66:67], v[66:67]
	v_rndne_f64_e32 v[68:69], v[68:69]
	v_fma_f64 v[46:47], v[46:47], s[16:17], -v[66:67]
	v_fma_f64 v[44:45], v[44:45], s[16:17], -v[68:69]
	v_cvt_f32_f64_e32 v47, v[46:47]
	v_cvt_f32_f64_e32 v45, v[44:45]
	v_cos_f32_e32 v46, v47
	v_sin_f32_e32 v44, v47
	v_cos_f32_e32 v47, v45
	v_sin_f32_e32 v45, v45
	v_lshlrev_b32_e32 v64, 16, v64
	v_lshlrev_b32_e32 v66, 16, v62
	v_and_b32_e32 v67, 0xffff0000, v62
	v_pk_mul_f32 v[62:63], v[44:45], v[64:65]
	s_lshl_b64 s[16:17], s[12:13], 7
	v_cndmask_b32_e64 v63, v63, -v63, s[4:5]
	v_cndmask_b32_e64 v62, v62, -v62, s[4:5]
	v_pk_fma_f32 v[62:63], v[46:47], v[66:67], v[62:63]
	s_nop 0
	v_cvt_pk_bf16_f32 v64, v62, v63
	v_lshl_add_u64 v[62:63], v[16:17], 0, s[16:17]
	global_store_dword v[62:63], v64, off
	s_and_b64 exec, exec, s[4:5]
	s_cbranch_execz .LBB0_245
	s_lshl_b64 s[12:13], s[12:13], 6
	v_lshl_add_u64 v[62:63], s[12:13], 2, v[24:25]
	global_store_dwordx2 v[62:63], v[46:47], off
	global_store_dwordx2 v[62:63], v[44:45], off offset:128

.LBB0_248:
	v_and_b32_e32 v45, 0xffff0000, v89
	v_and_b32_e32 v91, 0xffff0000, v87
	v_lshlrev_b32_e32 v44, 16, v89
	v_lshlrev_b32_e32 v46, 16, v88
	v_and_b32_e32 v47, 0xffff0000, v88
	v_lshlrev_b32_e32 v90, 16, v87
	v_mov_b32_e32 v94, v45
	v_mov_b32_e32 v95, v91
	v_pk_mul_f32 v[88:89], v[46:47], v[46:47]
	v_pk_mul_f32 v[94:95], v[94:95], v[94:95]
	v_mov_b32_e32 v96, v44
	v_mov_b32_e32 v97, v90
	s_waitcnt lgkmcnt(0)
	v_lshlrev_b32_e32 v92, 16, v86
	v_and_b32_e32 v93, 0xffff0000, v86
	v_lshlrev_b32_e32 v86, 16, v85
	v_and_b32_e32 v87, 0xffff0000, v85
	v_pk_fma_f32 v[94:95], v[96:97], v[96:97], v[94:95]
	v_add_f32_e32 v85, v88, v89
	v_add_f32_e32 v85, v94, v85
	v_add_f32_e32 v85, v85, v95
	s_ashr_i32 s19, s18, 31
	s_nop 0
	v_add_f32_dpp v85, v85, v85 quad_perm:[1,0,3,2] row_mask:0xf bank_mask:0xf bound_ctrl:1
	s_nop 1
	v_add_f32_dpp v85, v85, v85 quad_perm:[2,3,0,1] row_mask:0xf bank_mask:0xf bound_ctrl:1
	s_nop 1
	v_add_f32_dpp v85, v85, v85 row_half_mirror row_mask:0xf bank_mask:0xf bound_ctrl:1
	s_nop 1
	v_add_f32_dpp v85, v85, v85 row_mirror row_mask:0xf bank_mask:0xf bound_ctrl:1
	s_nop 0
	v_readlane_b32 s7, v85, 16
	v_readlane_b32 s9, v85, 48
	v_readlane_b32 s20, v85, 0
	v_readlane_b32 s21, v85, 32
	v_mov_b32_e32 v88, s7
	v_mov_b32_e32 v89, s9
	v_pk_add_f32 v[88:89], s[20:21], v[88:89]
	v_mad_i64_i32 v[94:95], s[20:21], s18, v193, v[20:21]
	v_add_f32_e32 v85, v88, v89
	v_fmamk_f32 v85, v85, 0x3b2aaaab, v189
	v_rsq_f32_e32 v88, v85
	s_nop 0
	v_pk_mul_f32 v[44:45], v[88:89], v[44:45] op_sel_hi:[0,1]
	v_pk_mul_f32 v[44:45], v[2:3], v[44:45]
	s_nop 0
	v_cvt_pk_bf16_f32 v44, v44, v45
	global_store_dword v[94:95], v44, off
	v_pk_mul_f32 v[44:45], v[88:89], v[46:47] op_sel_hi:[0,1]
	v_pk_mul_f32 v[44:45], v[4:5], v[44:45]
	v_mov_b32_e32 v46, v93
	v_cvt_pk_bf16_f32 v44, v44, v45
	global_store_dword v[94:95], v44, off offset:256
	v_pk_mul_f32 v[44:45], v[88:89], v[90:91] op_sel_hi:[0,1]
	v_pk_mul_f32 v[44:45], v[6:7], v[44:45]
	v_mov_b32_e32 v47, v87
	v_cvt_pk_bf16_f32 v85, v44, v45
	v_mov_b32_e32 v44, v92
	v_mov_b32_e32 v45, v86
	v_pk_mul_f32 v[46:47], v[46:47], v[46:47]
	global_store_dword v[94:95], v85, off offset:512
	v_pk_fma_f32 v[44:45], v[44:45], v[44:45], v[46:47]
	ds_bpermute_b32 v85, v1, v78
	v_add_f32_e32 v44, v44, v45
	s_nop 1
	v_add_f32_dpp v44, v44, v44 quad_perm:[1,0,3,2] row_mask:0xf bank_mask:0xf bound_ctrl:1
	s_nop 1
	v_add_f32_dpp v44, v44, v44 quad_perm:[2,3,0,1] row_mask:0xf bank_mask:0xf bound_ctrl:1
	s_nop 1
	v_add_f32_dpp v44, v44, v44 row_half_mirror row_mask:0xf bank_mask:0xf bound_ctrl:1
	s_nop 1
	v_add_f32_dpp v44, v44, v44 row_mirror row_mask:0xf bank_mask:0xf bound_ctrl:1
	s_nop 0
	v_readlane_b32 s7, v44, 16
	v_readlane_b32 s9, v44, 48
	v_readlane_b32 s20, v44, 0
	v_readlane_b32 s21, v44, 32
	v_mov_b32_e32 v44, s7
	v_mov_b32_e32 v45, s9
	v_pk_add_f32 v[44:45], s[20:21], v[44:45]
	s_lshl_b64 s[20:21], s[18:19], 9
	v_add_f32_e32 v44, v44, v45
	v_fmamk_f32 v44, v44, 0x3b800000, v189
	v_rsq_f32_e32 v44, v44
	v_lshl_add_u64 v[46:47], v[22:23], 0, s[20:21]
	v_pk_mul_f32 v[88:89], v[44:45], v[92:93] op_sel_hi:[0,1]
	v_pk_mul_f32 v[88:89], v[8:9], v[88:89]
	s_nop 0
	v_cvt_pk_bf16_f32 v45, v88, v89
	global_store_dword v[46:47], v45, off
	v_pk_mul_f32 v[44:45], v[44:45], v[86:87] op_sel_hi:[0,1]
	v_pk_mul_f32 v[44:45], v[10:11], v[44:45]
	s_nop 0
	v_cvt_pk_bf16_f32 v44, v44, v45
	global_store_dword v[46:47], v44, off offset:256
	s_and_saveexec_b64 s[20:21], s[2:3]
	s_cbranch_execz .LBB0_251
	v_cvt_f32_i32_e32 v44, v79
	s_mov_b32 s24, 0x6dc9c883
	s_mov_b32 s25, 0x3fc45f30
	v_cvt_f64_f32_e32 v[44:45], v44
	v_mul_f64 v[46:47], v[12:13], v[44:45]
	v_mul_f64 v[44:45], v[14:15], v[44:45]
	v_mul_f64 v[86:87], v[46:47], s[24:25]
	v_mul_f64 v[88:89], v[44:45], s[24:25]
	v_rndne_f64_e32 v[86:87], v[86:87]
	v_rndne_f64_e32 v[88:89], v[88:89]
	v_fma_f64 v[46:47], v[46:47], s[24:25], -v[86:87]
	v_fma_f64 v[44:45], v[44:45], s[24:25], -v[88:89]
	v_cvt_f32_f64_e32 v47, v[46:47]
	v_cvt_f32_f64_e32 v45, v[44:45]
	v_cos_f32_e32 v46, v47
	v_sin_f32_e32 v44, v47
	v_cos_f32_e32 v47, v45
	v_sin_f32_e32 v45, v45
	s_waitcnt lgkmcnt(0)
	v_and_b32_e32 v87, 0xffff0000, v85
	v_lshlrev_b32_e32 v86, 16, v85
	v_lshlrev_b32_e32 v88, 16, v78
	v_and_b32_e32 v89, 0xffff0000, v78
	v_pk_mul_f32 v[78:79], v[44:45], v[86:87]
	s_lshl_b64 s[24:25], s[18:19], 7
	v_cndmask_b32_e64 v79, v79, -v79, s[4:5]
	v_cndmask_b32_e64 v78, v78, -v78, s[4:5]
	v_pk_fma_f32 v[78:79], v[46:47], v[88:89], v[78:79]
	s_nop 0
	v_cvt_pk_bf16_f32 v85, v78, v79
	v_lshl_add_u64 v[78:79], v[16:17], 0, s[24:25]
	global_store_dword v[78:79], v85, off
	s_and_b64 exec, exec, s[4:5]
	s_cbranch_execz .LBB0_251
	s_lshl_b64 s[18:19], s[18:19], 6
	v_lshl_add_u64 v[78:79], s[18:19], 2, v[24:25]
	global_store_dwordx2 v[78:79], v[46:47], off
	global_store_dwordx2 v[78:79], v[44:45], off offset:128

.LBB0_253:
	v_and_b32_e32 v45, 0xffff0000, v75
	v_and_b32_e32 v77, 0xffff0000, v73
	v_lshlrev_b32_e32 v44, 16, v75
	v_lshlrev_b32_e32 v46, 16, v74
	v_and_b32_e32 v47, 0xffff0000, v74
	v_lshlrev_b32_e32 v76, 16, v73
	v_mov_b32_e32 v80, v45
	v_mov_b32_e32 v81, v77
	v_pk_mul_f32 v[74:75], v[46:47], v[46:47]
	v_pk_mul_f32 v[80:81], v[80:81], v[80:81]
	v_mov_b32_e32 v82, v44
	v_mov_b32_e32 v83, v76
	s_waitcnt lgkmcnt(0)
	v_lshlrev_b32_e32 v78, 16, v72
	v_and_b32_e32 v79, 0xffff0000, v72
	v_lshlrev_b32_e32 v72, 16, v71
	v_and_b32_e32 v73, 0xffff0000, v71
	v_pk_fma_f32 v[80:81], v[82:83], v[82:83], v[80:81]
	v_add_f32_e32 v71, v74, v75
	v_add_f32_e32 v71, v80, v71
	v_add_f32_e32 v71, v71, v81
	s_ashr_i32 s15, s14, 31
	s_nop 0
	v_add_f32_dpp v71, v71, v71 quad_perm:[1,0,3,2] row_mask:0xf bank_mask:0xf bound_ctrl:1
	s_nop 1
	v_add_f32_dpp v71, v71, v71 quad_perm:[2,3,0,1] row_mask:0xf bank_mask:0xf bound_ctrl:1
	s_nop 1
	v_add_f32_dpp v71, v71, v71 row_half_mirror row_mask:0xf bank_mask:0xf bound_ctrl:1
	s_nop 1
	v_add_f32_dpp v71, v71, v71 row_mirror row_mask:0xf bank_mask:0xf bound_ctrl:1
	s_nop 0
	v_readlane_b32 s7, v71, 16
	v_readlane_b32 s9, v71, 48
	v_readlane_b32 s16, v71, 0
	v_readlane_b32 s17, v71, 32
	v_mov_b32_e32 v74, s7
	v_mov_b32_e32 v75, s9
	v_pk_add_f32 v[74:75], s[16:17], v[74:75]
	v_mad_i64_i32 v[80:81], s[16:17], s14, v193, v[20:21]
	v_add_f32_e32 v71, v74, v75
	v_fmamk_f32 v71, v71, 0x3b2aaaab, v189
	v_rsq_f32_e32 v74, v71
	s_nop 0
	v_pk_mul_f32 v[44:45], v[74:75], v[44:45] op_sel_hi:[0,1]
	v_pk_mul_f32 v[44:45], v[2:3], v[44:45]
	s_nop 0
	v_cvt_pk_bf16_f32 v44, v44, v45
	global_store_dword v[80:81], v44, off
	v_pk_mul_f32 v[44:45], v[74:75], v[46:47] op_sel_hi:[0,1]
	v_pk_mul_f32 v[44:45], v[4:5], v[44:45]
	v_mov_b32_e32 v46, v79
	v_cvt_pk_bf16_f32 v44, v44, v45
	global_store_dword v[80:81], v44, off offset:256
	v_pk_mul_f32 v[44:45], v[74:75], v[76:77] op_sel_hi:[0,1]
	v_pk_mul_f32 v[44:45], v[6:7], v[44:45]
	v_mov_b32_e32 v47, v73
	v_cvt_pk_bf16_f32 v71, v44, v45
	v_mov_b32_e32 v44, v78
	v_mov_b32_e32 v45, v72
	v_pk_mul_f32 v[46:47], v[46:47], v[46:47]
	global_store_dword v[80:81], v71, off offset:512
	v_pk_fma_f32 v[44:45], v[44:45], v[44:45], v[46:47]
	ds_bpermute_b32 v71, v1, v69
	v_add_f32_e32 v44, v44, v45
	s_nop 1
	v_add_f32_dpp v44, v44, v44 quad_perm:[1,0,3,2] row_mask:0xf bank_mask:0xf bound_ctrl:1
	s_nop 1
	v_add_f32_dpp v44, v44, v44 quad_perm:[2,3,0,1] row_mask:0xf bank_mask:0xf bound_ctrl:1
	s_nop 1
	v_add_f32_dpp v44, v44, v44 row_half_mirror row_mask:0xf bank_mask:0xf bound_ctrl:1
	s_nop 1
	v_add_f32_dpp v44, v44, v44 row_mirror row_mask:0xf bank_mask:0xf bound_ctrl:1
	s_nop 0
	v_readlane_b32 s7, v44, 16
	v_readlane_b32 s9, v44, 48
	v_readlane_b32 s16, v44, 0
	v_readlane_b32 s17, v44, 32
	v_mov_b32_e32 v44, s7
	v_mov_b32_e32 v45, s9
	v_pk_add_f32 v[44:45], s[16:17], v[44:45]
	s_lshl_b64 s[16:17], s[14:15], 9
	v_add_f32_e32 v44, v44, v45
	v_fmamk_f32 v44, v44, 0x3b800000, v189
	v_rsq_f32_e32 v44, v44
	v_lshl_add_u64 v[46:47], v[22:23], 0, s[16:17]
	v_pk_mul_f32 v[74:75], v[44:45], v[78:79] op_sel_hi:[0,1]
	v_pk_mul_f32 v[74:75], v[8:9], v[74:75]
	s_nop 0
	v_cvt_pk_bf16_f32 v45, v74, v75
	global_store_dword v[46:47], v45, off
	v_pk_mul_f32 v[44:45], v[44:45], v[72:73] op_sel_hi:[0,1]
	v_pk_mul_f32 v[44:45], v[10:11], v[44:45]
	s_nop 0
	v_cvt_pk_bf16_f32 v44, v44, v45
	global_store_dword v[46:47], v44, off offset:256
	s_and_saveexec_b64 s[16:17], s[2:3]
	s_cbranch_execz .LBB0_256
	v_cvt_f32_i32_e32 v44, v70
	s_mov_b32 s18, 0x6dc9c883
	s_mov_b32 s19, 0x3fc45f30
	v_lshlrev_b32_e32 v70, 16, v69
	v_cvt_f64_f32_e32 v[44:45], v44
	v_mul_f64 v[46:47], v[12:13], v[44:45]
	v_mul_f64 v[44:45], v[14:15], v[44:45]
	v_mul_f64 v[72:73], v[46:47], s[18:19]
	v_mul_f64 v[74:75], v[44:45], s[18:19]
	v_rndne_f64_e32 v[72:73], v[72:73]
	v_rndne_f64_e32 v[74:75], v[74:75]
	v_fma_f64 v[46:47], v[46:47], s[18:19], -v[72:73]
	v_fma_f64 v[44:45], v[44:45], s[18:19], -v[74:75]
	v_cvt_f32_f64_e32 v47, v[46:47]
	v_cvt_f32_f64_e32 v45, v[44:45]
	v_cos_f32_e32 v46, v47
	v_sin_f32_e32 v44, v47
	v_cos_f32_e32 v47, v45
	v_sin_f32_e32 v45, v45
	s_waitcnt lgkmcnt(0)
	v_and_b32_e32 v73, 0xffff0000, v71
	v_lshlrev_b32_e32 v72, 16, v71
	v_and_b32_e32 v71, 0xffff0000, v69
	v_pk_mul_f32 v[72:73], v[44:45], v[72:73]
	s_lshl_b64 s[18:19], s[14:15], 7
	v_cndmask_b32_e64 v73, v73, -v73, s[4:5]
	v_cndmask_b32_e64 v72, v72, -v72, s[4:5]
	v_pk_fma_f32 v[70:71], v[46:47], v[70:71], v[72:73]
	s_nop 0
	v_cvt_pk_bf16_f32 v69, v70, v71
	v_lshl_add_u64 v[70:71], v[16:17], 0, s[18:19]
	global_store_dword v[70:71], v69, off
	s_and_b64 exec, exec, s[4:5]
	s_cbranch_execz .LBB0_256
	s_lshl_b64 s[14:15], s[14:15], 6
	v_lshl_add_u64 v[70:71], s[14:15], 2, v[24:25]
	global_store_dwordx2 v[70:71], v[46:47], off
	global_store_dwordx2 v[70:71], v[44:45], off offset:128

.LBB0_258:
	v_and_b32_e32 v45, 0xffff0000, v61
	v_and_b32_e32 v63, 0xffff0000, v59
	v_lshlrev_b32_e32 v44, 16, v61
	v_lshlrev_b32_e32 v46, 16, v60
	v_and_b32_e32 v47, 0xffff0000, v60
	v_lshlrev_b32_e32 v62, 16, v59
	v_mov_b32_e32 v66, v45
	v_mov_b32_e32 v67, v63
	v_pk_mul_f32 v[60:61], v[46:47], v[46:47]
	v_pk_mul_f32 v[66:67], v[66:67], v[66:67]
	v_mov_b32_e32 v68, v44
	v_mov_b32_e32 v69, v62
	s_waitcnt lgkmcnt(0)
	v_lshlrev_b32_e32 v64, 16, v58
	v_and_b32_e32 v65, 0xffff0000, v58
	v_lshlrev_b32_e32 v58, 16, v57
	v_and_b32_e32 v59, 0xffff0000, v57
	v_pk_fma_f32 v[66:67], v[68:69], v[68:69], v[66:67]
	v_add_f32_e32 v57, v60, v61
	v_add_f32_e32 v57, v66, v57
	v_add_f32_e32 v57, v57, v67
	s_ashr_i32 s11, s10, 31
	s_nop 0
	v_add_f32_dpp v57, v57, v57 quad_perm:[1,0,3,2] row_mask:0xf bank_mask:0xf bound_ctrl:1
	s_nop 1
	v_add_f32_dpp v57, v57, v57 quad_perm:[2,3,0,1] row_mask:0xf bank_mask:0xf bound_ctrl:1
	s_nop 1
	v_add_f32_dpp v57, v57, v57 row_half_mirror row_mask:0xf bank_mask:0xf bound_ctrl:1
	s_nop 1
	v_add_f32_dpp v57, v57, v57 row_mirror row_mask:0xf bank_mask:0xf bound_ctrl:1
	s_nop 0
	v_readlane_b32 s7, v57, 16
	v_readlane_b32 s9, v57, 48
	v_readlane_b32 s12, v57, 0
	v_readlane_b32 s13, v57, 32
	v_mov_b32_e32 v60, s7
	v_mov_b32_e32 v61, s9
	v_pk_add_f32 v[60:61], s[12:13], v[60:61]
	v_mad_i64_i32 v[66:67], s[12:13], s10, v193, v[20:21]
	v_add_f32_e32 v57, v60, v61
	v_fmamk_f32 v57, v57, 0x3b2aaaab, v189
	v_rsq_f32_e32 v60, v57
	s_nop 0
	v_pk_mul_f32 v[44:45], v[60:61], v[44:45] op_sel_hi:[0,1]
	v_pk_mul_f32 v[44:45], v[2:3], v[44:45]
	s_nop 0
	v_cvt_pk_bf16_f32 v44, v44, v45
	global_store_dword v[66:67], v44, off
	v_pk_mul_f32 v[44:45], v[60:61], v[46:47] op_sel_hi:[0,1]
	v_pk_mul_f32 v[44:45], v[4:5], v[44:45]
	v_mov_b32_e32 v46, v65
	v_cvt_pk_bf16_f32 v44, v44, v45
	global_store_dword v[66:67], v44, off offset:256
	v_pk_mul_f32 v[44:45], v[60:61], v[62:63] op_sel_hi:[0,1]
	v_pk_mul_f32 v[44:45], v[6:7], v[44:45]
	v_mov_b32_e32 v47, v59
	v_cvt_pk_bf16_f32 v57, v44, v45
	v_mov_b32_e32 v44, v64
	v_mov_b32_e32 v45, v58
	v_pk_mul_f32 v[46:47], v[46:47], v[46:47]
	global_store_dword v[66:67], v57, off offset:512
	v_pk_fma_f32 v[44:45], v[44:45], v[44:45], v[46:47]
	ds_bpermute_b32 v57, v1, v55
	v_add_f32_e32 v44, v44, v45
	s_nop 1
	v_add_f32_dpp v44, v44, v44 quad_perm:[1,0,3,2] row_mask:0xf bank_mask:0xf bound_ctrl:1
	s_nop 1
	v_add_f32_dpp v44, v44, v44 quad_perm:[2,3,0,1] row_mask:0xf bank_mask:0xf bound_ctrl:1
	s_nop 1
	v_add_f32_dpp v44, v44, v44 row_half_mirror row_mask:0xf bank_mask:0xf bound_ctrl:1
	s_nop 1
	v_add_f32_dpp v44, v44, v44 row_mirror row_mask:0xf bank_mask:0xf bound_ctrl:1
	s_nop 0
	v_readlane_b32 s7, v44, 16
	v_readlane_b32 s9, v44, 48
	v_readlane_b32 s12, v44, 0
	v_readlane_b32 s13, v44, 32
	v_mov_b32_e32 v44, s7
	v_mov_b32_e32 v45, s9
	v_pk_add_f32 v[44:45], s[12:13], v[44:45]
	s_lshl_b64 s[12:13], s[10:11], 9
	v_add_f32_e32 v44, v44, v45
	v_fmamk_f32 v44, v44, 0x3b800000, v189
	v_rsq_f32_e32 v44, v44
	v_lshl_add_u64 v[46:47], v[22:23], 0, s[12:13]
	v_pk_mul_f32 v[60:61], v[44:45], v[64:65] op_sel_hi:[0,1]
	v_pk_mul_f32 v[60:61], v[8:9], v[60:61]
	s_nop 0
	v_cvt_pk_bf16_f32 v45, v60, v61
	global_store_dword v[46:47], v45, off
	v_pk_mul_f32 v[44:45], v[44:45], v[58:59] op_sel_hi:[0,1]
	v_pk_mul_f32 v[44:45], v[10:11], v[44:45]
	s_nop 0
	v_cvt_pk_bf16_f32 v44, v44, v45
	global_store_dword v[46:47], v44, off offset:256
	s_and_saveexec_b64 s[12:13], s[2:3]
	s_cbranch_execz .LBB0_261
	v_cvt_f32_i32_e32 v44, v56
	s_mov_b32 s14, 0x6dc9c883
	s_mov_b32 s15, 0x3fc45f30
	v_lshlrev_b32_e32 v56, 16, v55
	v_cvt_f64_f32_e32 v[44:45], v44
	v_mul_f64 v[46:47], v[12:13], v[44:45]
	v_mul_f64 v[44:45], v[14:15], v[44:45]
	v_mul_f64 v[58:59], v[46:47], s[14:15]
	v_mul_f64 v[60:61], v[44:45], s[14:15]
	v_rndne_f64_e32 v[58:59], v[58:59]
	v_rndne_f64_e32 v[60:61], v[60:61]
	v_fma_f64 v[46:47], v[46:47], s[14:15], -v[58:59]
	v_fma_f64 v[44:45], v[44:45], s[14:15], -v[60:61]
	v_cvt_f32_f64_e32 v47, v[46:47]
	v_cvt_f32_f64_e32 v45, v[44:45]
	v_cos_f32_e32 v46, v47
	v_sin_f32_e32 v44, v47
	v_cos_f32_e32 v47, v45
	v_sin_f32_e32 v45, v45
	s_waitcnt lgkmcnt(0)
	v_and_b32_e32 v59, 0xffff0000, v57
	v_lshlrev_b32_e32 v58, 16, v57
	v_and_b32_e32 v57, 0xffff0000, v55
	v_pk_mul_f32 v[58:59], v[44:45], v[58:59]
	s_lshl_b64 s[14:15], s[10:11], 7
	v_cndmask_b32_e64 v59, v59, -v59, s[4:5]
	v_cndmask_b32_e64 v58, v58, -v58, s[4:5]
	v_pk_fma_f32 v[56:57], v[46:47], v[56:57], v[58:59]
	s_nop 0
	v_cvt_pk_bf16_f32 v55, v56, v57
	v_lshl_add_u64 v[56:57], v[16:17], 0, s[14:15]
	global_store_dword v[56:57], v55, off
	s_and_b64 exec, exec, s[4:5]
	s_cbranch_execz .LBB0_261
	s_lshl_b64 s[10:11], s[10:11], 6
	v_lshl_add_u64 v[56:57], s[10:11], 2, v[24:25]
	global_store_dwordx2 v[56:57], v[46:47], off
	global_store_dwordx2 v[56:57], v[44:45], off offset:128

.LBB0_262:
	v_and_b32_e32 v45, 0xffff0000, v54
	s_waitcnt lgkmcnt(0)
	v_and_b32_e32 v57, 0xffff0000, v52
	v_lshlrev_b32_e32 v44, 16, v54
	v_lshlrev_b32_e32 v46, 16, v53
	v_and_b32_e32 v47, 0xffff0000, v53
	v_lshlrev_b32_e32 v56, 16, v52
	v_lshlrev_b32_e32 v52, 16, v51
	v_and_b32_e32 v53, 0xffff0000, v51
	v_lshlrev_b32_e32 v58, 16, v50
	v_and_b32_e32 v59, 0xffff0000, v50
	v_mov_b32_e32 v50, v45
	v_mov_b32_e32 v51, v57
	v_pk_mul_f32 v[54:55], v[46:47], v[46:47]
	v_pk_mul_f32 v[50:51], v[50:51], v[50:51]
	v_mov_b32_e32 v60, v44
	v_mov_b32_e32 v61, v56
	v_pk_fma_f32 v[50:51], v[60:61], v[60:61], v[50:51]
	v_add_f32_e32 v54, v54, v55
	v_add_f32_e32 v50, v50, v54
	v_add_f32_e32 v50, v50, v51
	s_nop 1
	v_add_f32_dpp v50, v50, v50 quad_perm:[1,0,3,2] row_mask:0xf bank_mask:0xf bound_ctrl:1
	s_nop 1
	v_add_f32_dpp v50, v50, v50 quad_perm:[2,3,0,1] row_mask:0xf bank_mask:0xf bound_ctrl:1
	s_nop 1
	v_add_f32_dpp v50, v50, v50 row_half_mirror row_mask:0xf bank_mask:0xf bound_ctrl:1
	s_nop 1
	v_add_f32_dpp v50, v50, v50 row_mirror row_mask:0xf bank_mask:0xf bound_ctrl:1
	s_nop 0
	v_readlane_b32 s7, v50, 16
	v_readlane_b32 s9, v50, 48
	v_readlane_b32 s10, v50, 0
	v_readlane_b32 s11, v50, 32
	v_mov_b32_e32 v50, s7
	v_mov_b32_e32 v51, s9
	v_pk_add_f32 v[50:51], s[10:11], v[50:51]
	v_mad_i64_i32 v[54:55], s[10:11], s8, v193, v[20:21]
	v_add_f32_e32 v50, v50, v51
	v_fmamk_f32 v50, v50, 0x3b2aaaab, v189
	v_rsq_f32_e32 v50, v50
	s_ashr_i32 s9, s8, 31
	v_pk_mul_f32 v[44:45], v[50:51], v[44:45] op_sel_hi:[0,1]
	v_pk_mul_f32 v[44:45], v[2:3], v[44:45]
	s_nop 0
	v_cvt_pk_bf16_f32 v44, v44, v45
	global_store_dword v[54:55], v44, off
	v_pk_mul_f32 v[44:45], v[50:51], v[46:47] op_sel_hi:[0,1]
	v_pk_mul_f32 v[44:45], v[4:5], v[44:45]
	v_mov_b32_e32 v46, v53
	v_cvt_pk_bf16_f32 v44, v44, v45
	global_store_dword v[54:55], v44, off offset:256
	v_pk_mul_f32 v[44:45], v[50:51], v[56:57] op_sel_hi:[0,1]
	v_pk_mul_f32 v[44:45], v[6:7], v[44:45]
	v_mov_b32_e32 v47, v59
	v_cvt_pk_bf16_f32 v50, v44, v45
	v_mov_b32_e32 v44, v52
	v_mov_b32_e32 v45, v58
	v_pk_mul_f32 v[46:47], v[46:47], v[46:47]
	global_store_dword v[54:55], v50, off offset:512
	v_pk_fma_f32 v[44:45], v[44:45], v[44:45], v[46:47]
	s_nop 0
	v_add_f32_e32 v44, v44, v45
	s_nop 1
	v_add_f32_dpp v44, v44, v44 quad_perm:[1,0,3,2] row_mask:0xf bank_mask:0xf bound_ctrl:1
	s_nop 1
	v_add_f32_dpp v44, v44, v44 quad_perm:[2,3,0,1] row_mask:0xf bank_mask:0xf bound_ctrl:1
	s_nop 1
	v_add_f32_dpp v44, v44, v44 row_half_mirror row_mask:0xf bank_mask:0xf bound_ctrl:1
	s_nop 1
	v_add_f32_dpp v44, v44, v44 row_mirror row_mask:0xf bank_mask:0xf bound_ctrl:1
	s_nop 0
	v_readlane_b32 s7, v44, 16
	v_readlane_b32 s12, v44, 48
	v_readlane_b32 s10, v44, 0
	v_readlane_b32 s11, v44, 32
	v_mov_b32_e32 v44, s7
	v_mov_b32_e32 v45, s12
	v_pk_add_f32 v[44:45], s[10:11], v[44:45]
	s_lshl_b64 s[10:11], s[8:9], 9
	v_add_f32_e32 v44, v44, v45
	v_fmamk_f32 v44, v44, 0x3b800000, v189
	v_rsq_f32_e32 v44, v44
	v_lshl_add_u64 v[46:47], v[22:23], 0, s[10:11]
	v_pk_mul_f32 v[50:51], v[44:45], v[52:53] op_sel_hi:[0,1]
	v_pk_mul_f32 v[50:51], v[8:9], v[50:51]
	s_nop 0
	v_cvt_pk_bf16_f32 v45, v50, v51
	ds_bpermute_b32 v50, v1, v48
	global_store_dword v[46:47], v45, off
	v_pk_mul_f32 v[44:45], v[44:45], v[58:59] op_sel_hi:[0,1]
	v_pk_mul_f32 v[44:45], v[10:11], v[44:45]
	s_nop 0
	v_cvt_pk_bf16_f32 v44, v44, v45
	global_store_dword v[46:47], v44, off offset:256
	s_and_saveexec_b64 s[10:11], s[2:3]
	s_cbranch_execz .LBB0_226
	v_cvt_f32_i32_e32 v44, v49
	s_mov_b32 s12, 0x6dc9c883
	s_mov_b32 s13, 0x3fc45f30
	s_waitcnt lgkmcnt(0)
	v_and_b32_e32 v51, 0xffff0000, v50
	v_cvt_f64_f32_e32 v[44:45], v44
	v_mul_f64 v[46:47], v[12:13], v[44:45]
	v_mul_f64 v[44:45], v[14:15], v[44:45]
	v_mul_f64 v[52:53], v[46:47], s[12:13]
	v_mul_f64 v[54:55], v[44:45], s[12:13]
	v_rndne_f64_e32 v[52:53], v[52:53]
	v_rndne_f64_e32 v[54:55], v[54:55]
	v_fma_f64 v[46:47], v[46:47], s[12:13], -v[52:53]
	v_fma_f64 v[44:45], v[44:45], s[12:13], -v[54:55]
	v_cvt_f32_f64_e32 v47, v[46:47]
	v_cvt_f32_f64_e32 v45, v[44:45]
	v_cos_f32_e32 v46, v47
	v_sin_f32_e32 v44, v47
	v_cos_f32_e32 v47, v45
	v_sin_f32_e32 v45, v45
	v_lshlrev_b32_e32 v50, 16, v50
	v_lshlrev_b32_e32 v52, 16, v48
	v_and_b32_e32 v53, 0xffff0000, v48
	v_pk_mul_f32 v[48:49], v[44:45], v[50:51]
	s_lshl_b64 s[12:13], s[8:9], 7
	v_cndmask_b32_e64 v49, v49, -v49, s[4:5]
	v_cndmask_b32_e64 v48, v48, -v48, s[4:5]
	v_pk_fma_f32 v[48:49], v[46:47], v[52:53], v[48:49]
	s_nop 0
	v_cvt_pk_bf16_f32 v50, v48, v49
	v_lshl_add_u64 v[48:49], v[16:17], 0, s[12:13]
	global_store_dword v[48:49], v50, off
	s_and_b64 exec, exec, s[4:5]
	s_cbranch_execz .LBB0_226
	s_lshl_b64 s[8:9], s[8:9], 6
	v_lshl_add_u64 v[48:49], s[8:9], 2, v[24:25]
	global_store_dwordx2 v[48:49], v[46:47], off
	global_store_dwordx2 v[48:49], v[44:45], off offset:128
	s_branch .LBB0_226

.LBB0_680:
	s_or_b64 exec, exec, s[0:1]
	v_cndmask_b32_e32 v55, v84, v51, vcc
	v_cndmask_b32_e64 v56, v86, v51, s[4:5]
	v_sub_f32_e32 v57, v55, v55
	v_cndmask_b32_e64 v51, v88, v51, s[6:7]
	v_mul_f32_e32 v57, 0x3fb8aa3b, v57
	v_sub_f32_e32 v56, v56, v55
	v_exp_f32_e32 v57, v57
	v_mul_f32_e32 v56, 0x3fb8aa3b, v56
	v_sub_f32_e32 v51, v51, v55
	v_exp_f32_e32 v60, v56
	v_mul_f32_e32 v51, 0x3fb8aa3b, v51
	v_sub_f32_e32 v55, v80, v55
	v_exp_f32_e32 v51, v51
	v_mul_f32_e32 v55, 0x3fb8aa3b, v55
	v_exp_f32_e32 v62, v55
	v_add_f32_e32 v55, 0, v57
	v_add_f32_e32 v55, v55, v60
	v_add_f32_e32 v55, v55, v51
	v_add_f32_e32 v55, v55, v62
	v_div_scale_f32 v56, s[0:1], v55, v55, 1.0
	v_rcp_f32_e32 v58, v56
	v_readlane_b32 s0, v238, 4
	s_waitcnt lgkmcnt(0)
	v_fma_f32 v59, -v56, v58, 1.0
	v_fmac_f32_e32 v58, v59, v58
	v_div_scale_f32 v59, vcc, 1.0, v55, 1.0
	v_mul_f32_e32 v61, v59, v58
	v_fma_f32 v63, -v56, v61, v59
	v_fmac_f32_e32 v61, v63, v58
	v_fma_f32 v56, -v56, v61, v59
	v_div_fmas_f32 v56, v56, v58, v61
	v_lshl_add_u32 v58, v83, 2, s0
	ds_read_b32 v58, v58
	v_div_fixup_f32 v63, v56, v55, 1.0
	v_lshlrev_b32_e32 v55, 14, v83
	v_lshl_add_u32 v56, s74, 8, v34
	v_mul_f32_e32 v57, v63, v57
	s_waitcnt lgkmcnt(0)
	v_add3_u32 v54, v55, v58, v54
	v_ashrrev_i32_e32 v55, 31, v54
	v_lshl_add_u64 v[58:59], v[54:55], 3, s[82:83]
	v_add_u32_e32 v55, 0, v46
	v_add_u32_e32 v64, 0x22500, v55
	ds_write_b32 v64, v54
	v_lshl_add_u32 v54, v85, 2, s0
	ds_read_b32 v61, v54
	global_store_dwordx2 v[58:59], v[56:57], off
	v_lshlrev_b32_e32 v57, 14, v85
	v_mul_f32_e32 v55, v63, v60
	v_or_b32_e32 v54, 1, v56
	s_waitcnt lgkmcnt(0)
	v_add3_u32 v58, v57, v61, v53
	ds_write_b32 v64, v58 offset:4
	v_lshl_add_u32 v53, v87, 2, s0
	ds_read_b32 v53, v53
	v_ashrrev_i32_e32 v59, 31, v58
	v_lshl_add_u64 v[60:61], v[58:59], 3, s[82:83]
	global_store_dwordx2 v[60:61], v[54:55], off
	v_mul_f32_e32 v55, v63, v51
	v_lshlrev_b32_e32 v51, 14, v87
	s_waitcnt lgkmcnt(0)
	v_add3_u32 v52, v51, v53, v52
	ds_write_b32 v64, v52 offset:8
	v_lshl_add_u32 v51, v82, 2, s0
	ds_read_b32 v51, v51
	v_ashrrev_i32_e32 v53, 31, v52
	v_or_b32_e32 v54, 2, v56
	v_lshl_add_u64 v[58:59], v[52:53], 3, s[82:83]
	global_store_dwordx2 v[58:59], v[54:55], off
	v_lshlrev_b32_e32 v54, 14, v82
	s_waitcnt lgkmcnt(0)
	v_add3_u32 v50, v54, v51, v50
	v_ashrrev_i32_e32 v51, 31, v50
	v_mul_f32_e32 v53, v63, v62
	v_or_b32_e32 v52, 3, v56
	v_lshl_add_u64 v[54:55], v[50:51], 3, s[82:83]
	global_store_dwordx2 v[54:55], v[52:53], off
	ds_write_b32 v64, v50 offset:12
